# P3 epilogue: gate fetches of the second 128-row half issued with the first half's (one exposed latency, none behind the first half's stores)
# baseline (speedup 1.0000x reference)
.LBB0_895:
	v_add_u32_e32 v166, s83, v182
	v_ashrrev_i32_e32 v167, 31, v166
	v_add_u32_e32 v2, s84, v184
	v_lshlrev_b64 v[4:5], 11, v[166:167]
	s_nop 15
	s_nop 15
	v_lshl_add_u64 v[4:5], s[92:93], 0, v[4:5]
	v_ashrrev_i32_e32 v3, 31, v2
	v_lshl_add_u64 v[4:5], v[4:5], 0, v[2:3]
	global_load_dwordx2 v[168:169], v[4:5], off offset:1024 nt
	global_load_dwordx2 v[164:165], v[4:5], off offset:1152 nt
	v_add_co_u32_e32 v6, vcc, s74, v4
	v_lshlrev_b64 v[166:167], 10, v[166:167]
	s_nop 0
	v_addc_co_u32_e32 v7, vcc, 0, v5, vcc
	global_load_dwordx2 v[162:163], v[6:7], off offset:1024 nt
	global_load_dwordx2 v[160:161], v[6:7], off offset:1152 nt
	v_add_co_u32_e32 v6, vcc, s61, v4
	s_mov_b64 s[0:1], 0x4000
	s_nop 0
	v_addc_co_u32_e32 v7, vcc, 0, v5, vcc
	global_load_dwordx2 v[158:159], v[6:7], off offset:1024 nt
	global_load_dwordx2 v[156:157], v[6:7], off offset:1152 nt
	v_add_co_u32_e32 v252, vcc, s76, v4
	s_nop 1
	v_addc_co_u32_e32 v253, vcc, 0, v5, vcc
	global_load_dwordx2 v[236:237], v[252:253], off offset:1024 nt
	global_load_dwordx2 v[238:239], v[252:253], off offset:1152 nt
	v_add_co_u32_e32 v252, vcc, s77, v4
	s_nop 1
	v_addc_co_u32_e32 v253, vcc, 0, v5, vcc
	global_load_dwordx2 v[240:241], v[252:253], off offset:1024 nt
	global_load_dwordx2 v[242:243], v[252:253], off offset:1152 nt
	v_add_co_u32_e32 v252, vcc, s78, v4
	s_nop 1
	v_addc_co_u32_e32 v253, vcc, 0, v5, vcc
	global_load_dwordx2 v[244:245], v[252:253], off offset:1024 nt
	global_load_dwordx2 v[246:247], v[252:253], off offset:1152 nt
	v_add_co_u32_e32 v252, vcc, s79, v4
	s_nop 1
	v_addc_co_u32_e32 v253, vcc, 0, v5, vcc
	global_load_dwordx2 v[248:249], v[252:253], off offset:1024 nt
	global_load_dwordx2 v[250:251], v[252:253], off offset:1152 nt
	v_add_co_u32_e32 v6, vcc, s73, v4
	s_waitcnt vmcnt(0)
	v_cvt_pk_f32_fp8_e32 v[170:171], v168
	v_cvt_pk_f32_fp8_sdwa v[172:173], v168 src0_sel:WORD_1
	v_cvt_pk_f32_fp8_e32 v[174:175], v169
	v_cvt_pk_f32_fp8_sdwa v[168:169], v169 src0_sel:WORD_1
	v_mul_f32_e32 v11, 0xbfb8aa3b, v170
	v_min_f32_e32 v11, 0x42700000, v11
	v_exp_f32_e32 v11, v11
	v_mul_f32_e32 v170, 0xbfb8aa3b, v171
	v_min_f32_e32 v170, 0x42700000, v170
	v_exp_f32_e32 v170, v170
	v_add_f32_e32 v11, 1.0, v11
	v_rcp_f32_e32 v11, v11
	v_mul_f32_e32 v171, 0xbfb8aa3b, v172
	v_min_f32_e32 v171, 0x42700000, v171
	v_exp_f32_e32 v171, v171
	v_mul_f32_e32 v11, v136, v11
	v_add_f32_e32 v136, 1.0, v170
	v_rcp_f32_e32 v136, v136
	v_mul_f32_e32 v172, 0xbfb8aa3b, v173
	v_min_f32_e32 v172, 0x42700000, v172
	v_exp_f32_e32 v172, v172
	v_mul_f32_e32 v136, v137, v136
	v_add_f32_e32 v137, 1.0, v171
	v_rcp_f32_e32 v137, v137
	v_mul_f32_e32 v173, 0xbfb8aa3b, v174
	v_min_f32_e32 v173, 0x42700000, v173
	v_exp_f32_e32 v173, v173
	v_mul_f32_e32 v137, v138, v137
	v_add_f32_e32 v138, 1.0, v172
	v_rcp_f32_e32 v138, v138
	v_mul_f32_e32 v174, 0xbfb8aa3b, v175
	v_min_f32_e32 v174, 0x42700000, v174
	v_exp_f32_e32 v174, v174
	v_mul_f32_e32 v138, v139, v138
	v_add_f32_e32 v139, 1.0, v173
	v_rcp_f32_e32 v139, v139
	v_mul_f32_e32 v168, 0xbfb8aa3b, v168
	v_min_f32_e32 v168, 0x42700000, v168
	v_exp_f32_e32 v168, v168
	v_mul_f32_e32 v139, v132, v139
	v_add_f32_e32 v132, 1.0, v174
	v_rcp_f32_e32 v132, v132
	v_mul_f32_e32 v169, 0xbfb8aa3b, v169
	v_min_f32_e32 v169, 0x42700000, v169
	v_exp_f32_e32 v169, v169
	v_mul_f32_e32 v170, v133, v132
	v_add_f32_e32 v132, 1.0, v168
	v_rcp_f32_e32 v132, v132
	v_mov_b32_e32 v133, 0
	v_cvt_pk_fp8_f32 v133, v139, v170
	v_addc_co_u32_e32 v7, vcc, 0, v5, vcc
	v_mul_f32_e32 v134, v134, v132
	v_add_f32_e32 v132, 1.0, v169
	v_rcp_f32_e32 v132, v132
	global_load_dwordx2 v[8:9], v[6:7], off offset:1024 nt
	s_nop 0
	global_load_dwordx2 v[6:7], v[6:7], off offset:1152 nt
	v_mul_f32_e32 v135, v135, v132
	v_mov_b32_e32 v132, 0
	v_cvt_pk_fp8_f32 v132, v11, v136
	v_cvt_pk_fp8_f32 v133, v134, v135 op_sel:[0,0,1]
	v_lshl_add_u64 v[134:135], s[24:25], 0, v[166:167]
	v_lshl_add_u64 v[2:3], v[134:135], 0, v[2:3]
	v_cvt_pk_fp8_f32 v132, v137, v138 op_sel:[0,0,1]
	v_cvt_pk_f32_fp8_e32 v[136:137], v164
	v_cvt_pk_f32_fp8_sdwa v[138:139], v164 src0_sel:WORD_1
	v_cvt_pk_f32_fp8_e32 v[134:135], v165
	global_store_dwordx2 v[2:3], v[132:133], off
	v_mul_f32_e32 v11, 0xbfb8aa3b, v136
	v_min_f32_e32 v11, 0x42700000, v11
	v_exp_f32_e32 v11, v11
	v_mul_f32_e32 v136, 0xbfb8aa3b, v137
	v_min_f32_e32 v136, 0x42700000, v136
	v_exp_f32_e32 v136, v136
	v_add_f32_e32 v11, 1.0, v11
	v_rcp_f32_e32 v11, v11
	v_mul_f32_e32 v137, 0xbfb8aa3b, v138
	v_min_f32_e32 v137, 0x42700000, v137
	v_exp_f32_e32 v137, v137
	v_mul_f32_e32 v11, v128, v11
	v_add_f32_e32 v128, 1.0, v136
	v_rcp_f32_e32 v128, v128
	v_mul_f32_e32 v138, 0xbfb8aa3b, v139
	v_min_f32_e32 v138, 0x42700000, v138
	v_exp_f32_e32 v138, v138
	v_mul_f32_e32 v128, v129, v128
	v_add_f32_e32 v129, 1.0, v137
	v_rcp_f32_e32 v129, v129
	v_mul_f32_e32 v134, 0xbfb8aa3b, v134
	v_min_f32_e32 v134, 0x42700000, v134
	v_exp_f32_e32 v134, v134
	v_mul_f32_e32 v129, v130, v129
	v_add_f32_e32 v130, 1.0, v138
	v_rcp_f32_e32 v130, v130
	v_mul_f32_e32 v135, 0xbfb8aa3b, v135
	v_cvt_pk_f32_fp8_sdwa v[132:133], v165 src0_sel:WORD_1
	v_min_f32_e32 v135, 0x42700000, v135
	v_mul_f32_e32 v130, v131, v130
	v_add_f32_e32 v131, 1.0, v134
	v_exp_f32_e32 v135, v135
	v_rcp_f32_e32 v131, v131
	v_mul_f32_e32 v132, 0xbfb8aa3b, v132
	v_min_f32_e32 v132, 0x42700000, v132
	v_exp_f32_e32 v132, v132
	v_mul_f32_e32 v131, v124, v131
	v_add_f32_e32 v124, 1.0, v135
	v_rcp_f32_e32 v124, v124
	v_mul_f32_e32 v133, 0xbfb8aa3b, v133
	v_min_f32_e32 v133, 0x42700000, v133
	v_exp_f32_e32 v133, v133
	v_mul_f32_e32 v134, v125, v124
	v_add_f32_e32 v124, 1.0, v132
	v_rcp_f32_e32 v124, v124
	v_mov_b32_e32 v125, 0
	v_cvt_pk_fp8_f32 v125, v131, v134
	v_mul_f32_e32 v126, v126, v124
	v_add_f32_e32 v124, 1.0, v133
	v_rcp_f32_e32 v124, v124
	s_nop 0
	v_mul_f32_e32 v127, v127, v124
	v_mov_b32_e32 v124, 0
	v_cvt_pk_fp8_f32 v124, v11, v128
	v_cvt_pk_fp8_f32 v125, v126, v127 op_sel:[0,0,1]
	v_cvt_pk_f32_fp8_sdwa v[126:127], v162 src0_sel:WORD_1
	v_cvt_pk_fp8_f32 v124, v129, v130 op_sel:[0,0,1]
	v_cvt_pk_f32_fp8_e32 v[128:129], v163
	v_cvt_pk_f32_fp8_sdwa v[130:131], v163 src0_sel:WORD_1
	global_store_dwordx2 v[2:3], v[124:125], off offset:128
	v_cvt_pk_f32_fp8_e32 v[124:125], v162
	v_mul_f32_e32 v11, 0xbfb8aa3b, v124
	v_min_f32_e32 v11, 0x42700000, v11
	v_exp_f32_e32 v11, v11
	v_mul_f32_e32 v124, 0xbfb8aa3b, v125
	v_min_f32_e32 v124, 0x42700000, v124
	v_exp_f32_e32 v124, v124
	v_add_f32_e32 v11, 1.0, v11
	v_rcp_f32_e32 v11, v11
	v_mul_f32_e32 v125, 0xbfb8aa3b, v126
	v_min_f32_e32 v125, 0x42700000, v125
	v_exp_f32_e32 v125, v125
	v_mul_f32_e32 v11, v120, v11
	v_add_f32_e32 v120, 1.0, v124
	v_rcp_f32_e32 v120, v120
	v_mul_f32_e32 v126, 0xbfb8aa3b, v127
	v_min_f32_e32 v126, 0x42700000, v126
	v_exp_f32_e32 v126, v126
	v_mul_f32_e32 v120, v121, v120
	v_add_f32_e32 v121, 1.0, v125
	v_rcp_f32_e32 v121, v121
	v_mul_f32_e32 v127, 0xbfb8aa3b, v128
	v_min_f32_e32 v127, 0x42700000, v127
	v_exp_f32_e32 v127, v127
	v_mul_f32_e32 v121, v122, v121
	v_add_f32_e32 v122, 1.0, v126
	v_rcp_f32_e32 v122, v122
	v_mul_f32_e32 v128, 0xbfb8aa3b, v129
	v_min_f32_e32 v128, 0x42700000, v128
	v_exp_f32_e32 v128, v128
	v_mul_f32_e32 v122, v123, v122
	v_add_f32_e32 v123, 1.0, v127
	v_rcp_f32_e32 v123, v123
	v_mul_f32_e32 v129, 0xbfb8aa3b, v130
	v_min_f32_e32 v129, 0x42700000, v129
	v_exp_f32_e32 v129, v129
	v_mul_f32_e32 v123, v116, v123
	v_add_f32_e32 v116, 1.0, v128
	v_rcp_f32_e32 v116, v116
	v_mul_f32_e32 v130, 0xbfb8aa3b, v131
	v_min_f32_e32 v130, 0x42700000, v130
	v_exp_f32_e32 v130, v130
	v_mul_f32_e32 v124, v117, v116
	v_add_f32_e32 v116, 1.0, v129
	v_rcp_f32_e32 v116, v116
	v_mov_b32_e32 v117, 0
	v_cvt_pk_fp8_f32 v117, v123, v124
	v_cvt_pk_f32_fp8_sdwa v[124:125], v161 src0_sel:WORD_1
	v_mul_f32_e32 v118, v118, v116
	v_add_f32_e32 v116, 1.0, v130
	v_rcp_f32_e32 v116, v116
	s_nop 0
	v_mul_f32_e32 v119, v119, v116
	v_mov_b32_e32 v116, 0
	v_cvt_pk_fp8_f32 v116, v11, v120
	v_cvt_pk_fp8_f32 v117, v118, v119 op_sel:[0,0,1]
	v_lshl_add_u64 v[118:119], v[2:3], 0, s[0:1]
	s_movk_i32 s0, 0x4000
	v_cvt_pk_fp8_f32 v116, v121, v122 op_sel:[0,0,1]
	v_add_co_u32_e32 v120, vcc, s0, v2
	v_cvt_pk_f32_fp8_e32 v[122:123], v161
	s_nop 0
	v_addc_co_u32_e32 v121, vcc, 0, v3, vcc
	global_store_dwordx2 v[120:121], v[116:117], off
	v_cvt_pk_f32_fp8_e32 v[116:117], v160
	v_cvt_pk_f32_fp8_sdwa v[120:121], v160 src0_sel:WORD_1
	s_mov_b64 s[0:1], 0x8000
	v_mul_f32_e32 v11, 0xbfb8aa3b, v116
	v_min_f32_e32 v11, 0x42700000, v11
	v_exp_f32_e32 v11, v11
	v_mul_f32_e32 v116, 0xbfb8aa3b, v117
	v_min_f32_e32 v116, 0x42700000, v116
	v_exp_f32_e32 v116, v116
	v_add_f32_e32 v11, 1.0, v11
	v_rcp_f32_e32 v11, v11
	v_mul_f32_e32 v117, 0xbfb8aa3b, v120
	v_min_f32_e32 v117, 0x42700000, v117
	v_exp_f32_e32 v117, v117
	v_mul_f32_e32 v11, v112, v11
	v_add_f32_e32 v112, 1.0, v116
	v_rcp_f32_e32 v112, v112
	v_mul_f32_e32 v120, 0xbfb8aa3b, v121
	v_min_f32_e32 v120, 0x42700000, v120
	v_exp_f32_e32 v120, v120
	v_mul_f32_e32 v112, v113, v112
	v_add_f32_e32 v113, 1.0, v117
	v_rcp_f32_e32 v113, v113
	v_mul_f32_e32 v121, 0xbfb8aa3b, v122
	v_min_f32_e32 v121, 0x42700000, v121
	v_exp_f32_e32 v121, v121
	v_mul_f32_e32 v113, v114, v113
	v_add_f32_e32 v114, 1.0, v120
	v_rcp_f32_e32 v114, v114
	v_mul_f32_e32 v122, 0xbfb8aa3b, v123
	v_min_f32_e32 v122, 0x42700000, v122
	v_exp_f32_e32 v122, v122
	v_mul_f32_e32 v114, v115, v114
	v_add_f32_e32 v115, 1.0, v121
	v_rcp_f32_e32 v115, v115
	v_mul_f32_e32 v123, 0xbfb8aa3b, v124
	v_min_f32_e32 v123, 0x42700000, v123
	v_exp_f32_e32 v123, v123
	v_mul_f32_e32 v115, v108, v115
	v_add_f32_e32 v108, 1.0, v122
	v_rcp_f32_e32 v108, v108
	v_mul_f32_e32 v124, 0xbfb8aa3b, v125
	v_min_f32_e32 v124, 0x42700000, v124
	v_exp_f32_e32 v124, v124
	v_mul_f32_e32 v116, v109, v108
	v_add_f32_e32 v108, 1.0, v123
	v_rcp_f32_e32 v108, v108
	v_mov_b32_e32 v109, 0
	v_cvt_pk_fp8_f32 v109, v115, v116
	v_mul_f32_e32 v110, v110, v108
	v_add_f32_e32 v108, 1.0, v124
	v_rcp_f32_e32 v108, v108
	s_nop 0
	v_mul_f32_e32 v111, v111, v108
	v_mov_b32_e32 v108, 0
	v_cvt_pk_fp8_f32 v108, v11, v112
	v_cvt_pk_fp8_f32 v109, v110, v111 op_sel:[0,0,1]
	v_cvt_pk_f32_fp8_sdwa v[110:111], v158 src0_sel:WORD_1
	v_cvt_pk_fp8_f32 v108, v113, v114 op_sel:[0,0,1]
	v_cvt_pk_f32_fp8_e32 v[112:113], v159
	v_cvt_pk_f32_fp8_sdwa v[114:115], v159 src0_sel:WORD_1
	global_store_dwordx2 v[118:119], v[108:109], off offset:128
	v_cvt_pk_f32_fp8_e32 v[108:109], v158
	v_mul_f32_e32 v11, 0xbfb8aa3b, v108
	v_min_f32_e32 v11, 0x42700000, v11
	v_exp_f32_e32 v11, v11
	v_mul_f32_e32 v108, 0xbfb8aa3b, v109
	v_min_f32_e32 v108, 0x42700000, v108
	v_exp_f32_e32 v108, v108
	v_add_f32_e32 v11, 1.0, v11
	v_rcp_f32_e32 v11, v11
	v_mul_f32_e32 v109, 0xbfb8aa3b, v110
	v_min_f32_e32 v109, 0x42700000, v109
	v_exp_f32_e32 v109, v109
	v_mul_f32_e32 v11, v104, v11
	v_add_f32_e32 v104, 1.0, v108
	v_rcp_f32_e32 v104, v104
	v_mul_f32_e32 v110, 0xbfb8aa3b, v111
	v_min_f32_e32 v110, 0x42700000, v110
	v_exp_f32_e32 v110, v110
	v_mul_f32_e32 v104, v105, v104
	v_add_f32_e32 v105, 1.0, v109
	v_rcp_f32_e32 v105, v105
	v_mul_f32_e32 v111, 0xbfb8aa3b, v112
	v_min_f32_e32 v111, 0x42700000, v111
	v_exp_f32_e32 v111, v111
	v_mul_f32_e32 v105, v106, v105
	v_add_f32_e32 v106, 1.0, v110
	v_rcp_f32_e32 v106, v106
	v_mul_f32_e32 v112, 0xbfb8aa3b, v113
	v_min_f32_e32 v112, 0x42700000, v112
	v_exp_f32_e32 v112, v112
	v_mul_f32_e32 v106, v107, v106
	v_add_f32_e32 v107, 1.0, v111
	v_rcp_f32_e32 v107, v107
	v_mul_f32_e32 v113, 0xbfb8aa3b, v114
	v_min_f32_e32 v113, 0x42700000, v113
	v_exp_f32_e32 v113, v113
	v_mul_f32_e32 v107, v100, v107
	v_add_f32_e32 v100, 1.0, v112
	v_rcp_f32_e32 v100, v100
	v_mul_f32_e32 v114, 0xbfb8aa3b, v115
	v_min_f32_e32 v114, 0x42700000, v114
	v_exp_f32_e32 v114, v114
	v_mul_f32_e32 v108, v101, v100
	v_add_f32_e32 v100, 1.0, v113
	v_rcp_f32_e32 v100, v100
	v_mov_b32_e32 v101, 0
	v_cvt_pk_fp8_f32 v101, v107, v108
	v_cvt_pk_f32_fp8_sdwa v[108:109], v157 src0_sel:WORD_1
	v_mul_f32_e32 v102, v102, v100
	v_add_f32_e32 v100, 1.0, v114
	v_rcp_f32_e32 v100, v100
	s_nop 0
	v_mul_f32_e32 v103, v103, v100
	v_mov_b32_e32 v100, 0
	v_cvt_pk_fp8_f32 v100, v11, v104
	v_cvt_pk_fp8_f32 v101, v102, v103 op_sel:[0,0,1]
	v_add_co_u32_e32 v104, vcc, s74, v2
	v_cvt_pk_fp8_f32 v100, v105, v106 op_sel:[0,0,1]
	s_nop 0
	v_addc_co_u32_e32 v105, vcc, 0, v3, vcc
	v_cvt_pk_f32_fp8_e32 v[106:107], v157
	global_store_dwordx2 v[104:105], v[100:101], off
	v_cvt_pk_f32_fp8_e32 v[100:101], v156
	v_cvt_pk_f32_fp8_sdwa v[104:105], v156 src0_sel:WORD_1
	v_lshl_add_u64 v[102:103], v[2:3], 0, s[0:1]
	s_mov_b64 s[0:1], 0xc000
	v_mul_f32_e32 v11, 0xbfb8aa3b, v100
	v_min_f32_e32 v11, 0x42700000, v11
	v_exp_f32_e32 v11, v11
	v_mul_f32_e32 v100, 0xbfb8aa3b, v101
	v_min_f32_e32 v100, 0x42700000, v100
	v_exp_f32_e32 v100, v100
	v_add_f32_e32 v11, 1.0, v11
	v_rcp_f32_e32 v11, v11
	v_mul_f32_e32 v101, 0xbfb8aa3b, v104
	v_min_f32_e32 v101, 0x42700000, v101
	v_exp_f32_e32 v101, v101
	v_mul_f32_e32 v11, v96, v11
	v_add_f32_e32 v96, 1.0, v100
	v_rcp_f32_e32 v96, v96
	v_mul_f32_e32 v104, 0xbfb8aa3b, v105
	v_min_f32_e32 v104, 0x42700000, v104
	v_exp_f32_e32 v104, v104
	v_mul_f32_e32 v96, v97, v96
	v_add_f32_e32 v97, 1.0, v101
	v_rcp_f32_e32 v97, v97
	v_mul_f32_e32 v105, 0xbfb8aa3b, v106
	v_min_f32_e32 v105, 0x42700000, v105
	v_exp_f32_e32 v105, v105
	v_mul_f32_e32 v97, v98, v97
	v_add_f32_e32 v98, 1.0, v104
	v_rcp_f32_e32 v98, v98
	v_mul_f32_e32 v106, 0xbfb8aa3b, v107
	v_min_f32_e32 v106, 0x42700000, v106
	v_exp_f32_e32 v106, v106
	v_mul_f32_e32 v98, v99, v98
	v_add_f32_e32 v99, 1.0, v105
	v_rcp_f32_e32 v99, v99
	v_mul_f32_e32 v107, 0xbfb8aa3b, v108
	v_min_f32_e32 v107, 0x42700000, v107
	v_exp_f32_e32 v107, v107
	v_mul_f32_e32 v99, v92, v99
	v_add_f32_e32 v92, 1.0, v106
	v_rcp_f32_e32 v92, v92
	v_mul_f32_e32 v108, 0xbfb8aa3b, v109
	v_min_f32_e32 v108, 0x42700000, v108
	v_exp_f32_e32 v108, v108
	v_mul_f32_e32 v100, v93, v92
	v_add_f32_e32 v92, 1.0, v107
	v_rcp_f32_e32 v92, v92
	v_mov_b32_e32 v93, 0
	v_cvt_pk_fp8_f32 v93, v99, v100
	v_mul_f32_e32 v94, v94, v92
	v_add_f32_e32 v92, 1.0, v108
	v_rcp_f32_e32 v92, v92
	s_nop 0
	v_mul_f32_e32 v95, v95, v92
	v_mov_b32_e32 v92, 0
	v_cvt_pk_fp8_f32 v92, v11, v96
	v_cvt_pk_fp8_f32 v93, v94, v95 op_sel:[0,0,1]
	s_waitcnt vmcnt(0)
	v_cvt_pk_f32_fp8_sdwa v[94:95], v8 src0_sel:WORD_1
	v_cvt_pk_fp8_f32 v92, v97, v98 op_sel:[0,0,1]
	v_cvt_pk_f32_fp8_e32 v[96:97], v9
	global_store_dwordx2 v[102:103], v[92:93], off offset:128
	v_cvt_pk_f32_fp8_e32 v[92:93], v8
	v_cvt_pk_f32_fp8_sdwa v[8:9], v9 src0_sel:WORD_1
	v_mul_f32_e32 v11, 0xbfb8aa3b, v92
	v_min_f32_e32 v11, 0x42700000, v11
	v_exp_f32_e32 v11, v11
	v_mul_f32_e32 v92, 0xbfb8aa3b, v93
	v_min_f32_e32 v92, 0x42700000, v92
	v_exp_f32_e32 v92, v92
	v_add_f32_e32 v11, 1.0, v11
	v_rcp_f32_e32 v11, v11
	v_mul_f32_e32 v93, 0xbfb8aa3b, v94
	v_min_f32_e32 v93, 0x42700000, v93
	v_exp_f32_e32 v93, v93
	v_mul_f32_e32 v11, v88, v11
	v_add_f32_e32 v88, 1.0, v92
	v_rcp_f32_e32 v88, v88
	v_mul_f32_e32 v94, 0xbfb8aa3b, v95
	v_min_f32_e32 v94, 0x42700000, v94
	v_exp_f32_e32 v94, v94
	v_mul_f32_e32 v88, v89, v88
	v_add_f32_e32 v89, 1.0, v93
	v_rcp_f32_e32 v89, v89
	v_mul_f32_e32 v95, 0xbfb8aa3b, v96
	v_mul_f32_e32 v8, 0xbfb8aa3b, v8
	v_min_f32_e32 v95, 0x42700000, v95
	v_min_f32_e32 v8, 0x42700000, v8
	v_mul_f32_e32 v89, v90, v89
	v_add_f32_e32 v90, 1.0, v94
	v_exp_f32_e32 v95, v95
	v_exp_f32_e32 v8, v8
	v_rcp_f32_e32 v90, v90
	v_mul_f32_e32 v96, 0xbfb8aa3b, v97
	v_mul_f32_e32 v9, 0xbfb8aa3b, v9
	v_min_f32_e32 v96, 0x42700000, v96
	v_min_f32_e32 v9, 0x42700000, v9
	v_mul_f32_e32 v90, v91, v90
	v_add_f32_e32 v91, 1.0, v95
	v_add_f32_e32 v8, 1.0, v8
	v_exp_f32_e32 v96, v96
	v_exp_f32_e32 v9, v9
	v_rcp_f32_e32 v91, v91
	v_rcp_f32_e32 v8, v8
	v_mul_f32_e32 v84, v84, v91
	v_add_f32_e32 v91, 1.0, v96
	v_mul_f32_e32 v86, v86, v8
	v_add_f32_e32 v8, 1.0, v9
	v_rcp_f32_e32 v91, v91
	v_rcp_f32_e32 v8, v8
	v_mov_b32_e32 v9, 0
	v_mul_f32_e32 v85, v85, v91
	v_mul_f32_e32 v87, v87, v8
	v_mov_b32_e32 v8, 0
	v_cvt_pk_fp8_f32 v8, v11, v88
	v_cvt_pk_fp8_f32 v9, v84, v85
	v_lshl_add_u64 v[84:85], v[2:3], 0, s[0:1]
	s_mov_b32 s0, 0xc000
	v_cvt_pk_fp8_f32 v8, v89, v90 op_sel:[0,0,1]
	v_cvt_pk_fp8_f32 v9, v86, v87 op_sel:[0,0,1]
	v_add_co_u32_e32 v86, vcc, s0, v2
	v_cvt_pk_f32_fp8_e32 v[88:89], v7
	s_nop 0
	v_addc_co_u32_e32 v87, vcc, 0, v3, vcc
	global_store_dwordx2 v[86:87], v[8:9], off
	v_cvt_pk_f32_fp8_e32 v[8:9], v6
	v_cvt_pk_f32_fp8_sdwa v[86:87], v6 src0_sel:WORD_1
	v_cvt_pk_f32_fp8_sdwa v[6:7], v7 src0_sel:WORD_1
	s_mov_b64 s[0:1], 0x20000
	v_mul_f32_e32 v9, 0xbfb8aa3b, v9
	v_min_f32_e32 v9, 0x42700000, v9
	v_exp_f32_e32 v9, v9
	v_mul_f32_e32 v11, 0xbfb8aa3b, v86
	v_mul_f32_e32 v86, 0xbfb8aa3b, v87
	v_mul_f32_e32 v87, 0xbfb8aa3b, v88
	v_mul_f32_e32 v6, 0xbfb8aa3b, v6
	v_min_f32_e32 v87, 0x42700000, v87
	v_min_f32_e32 v6, 0x42700000, v6
	v_add_f32_e32 v9, 1.0, v9
	v_exp_f32_e32 v87, v87
	v_exp_f32_e32 v6, v6
	v_rcp_f32_e32 v9, v9
	v_mul_f32_e32 v8, 0xbfb8aa3b, v8
	v_min_f32_e32 v8, 0x42700000, v8
	v_mul_f32_e32 v88, 0xbfb8aa3b, v89
	v_mul_f32_e32 v7, 0xbfb8aa3b, v7
	v_exp_f32_e32 v8, v8
	v_min_f32_e32 v88, 0x42700000, v88
	v_min_f32_e32 v7, 0x42700000, v7
	v_mul_f32_e32 v9, v81, v9
	v_add_f32_e32 v81, 1.0, v87
	v_add_f32_e32 v6, 1.0, v6
	v_exp_f32_e32 v88, v88
	v_exp_f32_e32 v7, v7
	v_rcp_f32_e32 v81, v81
	v_rcp_f32_e32 v6, v6
	v_min_f32_e32 v11, 0x42700000, v11
	v_min_f32_e32 v86, 0x42700000, v86
	v_add_f32_e32 v8, 1.0, v8
	v_exp_f32_e32 v11, v11
	v_exp_f32_e32 v86, v86
	v_rcp_f32_e32 v8, v8
	v_mul_f32_e32 v76, v76, v81
	v_add_f32_e32 v81, 1.0, v88
	v_mul_f32_e32 v78, v78, v6
	v_add_f32_e32 v6, 1.0, v7
	v_rcp_f32_e32 v81, v81
	v_rcp_f32_e32 v6, v6
	v_mul_f32_e32 v8, v80, v8
	v_add_f32_e32 v11, 1.0, v11
	v_add_f32_e32 v80, 1.0, v86
	v_rcp_f32_e32 v11, v11
	v_rcp_f32_e32 v80, v80
	v_mul_f32_e32 v77, v77, v81
	v_mul_f32_e32 v79, v79, v6
	v_mov_b32_e32 v6, 0
	v_mov_b32_e32 v7, 0
	v_cvt_pk_fp8_f32 v6, v8, v9
	v_cvt_pk_fp8_f32 v7, v76, v77
	v_mul_f32_e32 v11, v82, v11
	v_mul_f32_e32 v80, v83, v80
	v_cvt_pk_fp8_f32 v6, v11, v80 op_sel:[0,0,1]
	v_cvt_pk_fp8_f32 v7, v78, v79 op_sel:[0,0,1]
	global_store_dwordx2 v[84:85], v[6:7], off offset:128
	v_add_co_u32_e32 v6, vcc, s76, v4
	s_nop 1
	v_addc_co_u32_e32 v7, vcc, 0, v5, vcc
	v_mov_b64_e32 v[82:83], v[236:237]
	v_mov_b64_e32 v[84:85], v[238:239]
	v_add_co_u32_e32 v6, vcc, s77, v4
	v_cvt_pk_f32_fp8_e32 v[86:87], v82
	v_cvt_pk_f32_fp8_sdwa v[88:89], v82 src0_sel:WORD_1
	v_cvt_pk_f32_fp8_e32 v[90:91], v83
	v_cvt_pk_f32_fp8_sdwa v[82:83], v83 src0_sel:WORD_1
	v_mul_f32_e32 v11, 0xbfb8aa3b, v86
	v_min_f32_e32 v11, 0x42700000, v11
	v_exp_f32_e32 v11, v11
	v_mul_f32_e32 v86, 0xbfb8aa3b, v87
	v_min_f32_e32 v86, 0x42700000, v86
	v_exp_f32_e32 v86, v86
	v_add_f32_e32 v11, 1.0, v11
	v_rcp_f32_e32 v11, v11
	v_mul_f32_e32 v87, 0xbfb8aa3b, v88
	v_min_f32_e32 v87, 0x42700000, v87
	v_exp_f32_e32 v87, v87
	v_mul_f32_e32 v11, v72, v11
	v_add_f32_e32 v72, 1.0, v86
	v_rcp_f32_e32 v72, v72
	v_mul_f32_e32 v88, 0xbfb8aa3b, v89
	v_min_f32_e32 v88, 0x42700000, v88
	v_exp_f32_e32 v88, v88
	v_mul_f32_e32 v72, v73, v72
	v_add_f32_e32 v73, 1.0, v87
	v_rcp_f32_e32 v73, v73
	v_mul_f32_e32 v89, 0xbfb8aa3b, v90
	v_min_f32_e32 v89, 0x42700000, v89
	v_exp_f32_e32 v89, v89
	v_mul_f32_e32 v73, v74, v73
	v_add_f32_e32 v74, 1.0, v88
	v_rcp_f32_e32 v74, v74
	v_mul_f32_e32 v90, 0xbfb8aa3b, v91
	v_min_f32_e32 v90, 0x42700000, v90
	v_exp_f32_e32 v90, v90
	v_mul_f32_e32 v74, v75, v74
	v_add_f32_e32 v75, 1.0, v89
	v_rcp_f32_e32 v75, v75
	v_mul_f32_e32 v82, 0xbfb8aa3b, v82
	v_min_f32_e32 v82, 0x42700000, v82
	v_exp_f32_e32 v82, v82
	v_mul_f32_e32 v75, v68, v75
	v_add_f32_e32 v68, 1.0, v90
	v_rcp_f32_e32 v68, v68
	v_addc_co_u32_e32 v7, vcc, 0, v5, vcc
	v_mov_b64_e32 v[80:81], v[240:241]
	v_mov_b64_e32 v[78:79], v[242:243]
	v_mul_f32_e32 v83, 0xbfb8aa3b, v83
	v_min_f32_e32 v83, 0x42700000, v83
	v_mul_f32_e32 v86, v69, v68
	v_add_f32_e32 v68, 1.0, v82
	v_exp_f32_e32 v83, v83
	v_rcp_f32_e32 v68, v68
	v_mov_b32_e32 v69, 0
	v_cvt_pk_fp8_f32 v69, v75, v86
	v_add_co_u32_e32 v6, vcc, s78, v4
	v_mul_f32_e32 v70, v70, v68
	v_add_f32_e32 v68, 1.0, v83
	v_rcp_f32_e32 v68, v68
	v_addc_co_u32_e32 v7, vcc, 0, v5, vcc
	v_add_co_u32_e32 v4, vcc, s79, v4
	v_mul_f32_e32 v71, v71, v68
	v_mov_b32_e32 v68, 0
	v_cvt_pk_fp8_f32 v68, v11, v72
	v_cvt_pk_fp8_f32 v69, v70, v71 op_sel:[0,0,1]
	v_addc_co_u32_e32 v5, vcc, 0, v5, vcc
	v_cvt_pk_fp8_f32 v68, v73, v74 op_sel:[0,0,1]
	v_lshl_add_u64 v[70:71], v[2:3], 0, s[0:1]
	s_mov_b32 s0, 0x20000
	v_add_co_u32_e32 v72, vcc, s0, v2
	v_mov_b64_e32 v[76:77], v[244:245]
	v_mov_b64_e32 v[8:9], v[246:247]
	v_addc_co_u32_e32 v73, vcc, 0, v3, vcc
	v_mov_b64_e32 v[6:7], v[248:249]
	s_nop 0
	v_mov_b64_e32 v[4:5], v[250:251]
	v_cvt_pk_f32_fp8_e32 v[74:75], v85
	global_store_dwordx2 v[72:73], v[68:69], off
	v_cvt_pk_f32_fp8_e32 v[68:69], v84
	v_cvt_pk_f32_fp8_sdwa v[72:73], v84 src0_sel:WORD_1
	v_cvt_pk_f32_fp8_sdwa v[82:83], v85 src0_sel:WORD_1
	s_mov_b64 s[0:1], 0x24000
	v_mul_f32_e32 v11, 0xbfb8aa3b, v68
	v_min_f32_e32 v11, 0x42700000, v11
	v_exp_f32_e32 v11, v11
	v_mul_f32_e32 v68, 0xbfb8aa3b, v69
	v_min_f32_e32 v68, 0x42700000, v68
	v_exp_f32_e32 v68, v68
	v_add_f32_e32 v11, 1.0, v11
	v_rcp_f32_e32 v11, v11
	v_mul_f32_e32 v69, 0xbfb8aa3b, v72
	v_min_f32_e32 v69, 0x42700000, v69
	v_exp_f32_e32 v69, v69
	v_mul_f32_e32 v11, v64, v11
	v_add_f32_e32 v64, 1.0, v68
	v_rcp_f32_e32 v64, v64
	v_mul_f32_e32 v72, 0xbfb8aa3b, v73
	v_min_f32_e32 v72, 0x42700000, v72
	v_exp_f32_e32 v72, v72
	v_mul_f32_e32 v64, v65, v64
	v_add_f32_e32 v65, 1.0, v69
	v_rcp_f32_e32 v65, v65
	v_mul_f32_e32 v73, 0xbfb8aa3b, v74
	v_min_f32_e32 v73, 0x42700000, v73
	v_exp_f32_e32 v73, v73
	v_mul_f32_e32 v65, v66, v65
	v_add_f32_e32 v66, 1.0, v72
	v_rcp_f32_e32 v66, v66
	v_mul_f32_e32 v74, 0xbfb8aa3b, v75
	v_min_f32_e32 v74, 0x42700000, v74
	v_exp_f32_e32 v74, v74
	v_mul_f32_e32 v66, v67, v66
	v_add_f32_e32 v67, 1.0, v73
	v_rcp_f32_e32 v67, v67
	v_mul_f32_e32 v75, 0xbfb8aa3b, v82
	v_min_f32_e32 v75, 0x42700000, v75
	v_exp_f32_e32 v75, v75
	v_mul_f32_e32 v67, v60, v67
	v_add_f32_e32 v60, 1.0, v74
	v_rcp_f32_e32 v60, v60
	v_mul_f32_e32 v82, 0xbfb8aa3b, v83
	v_min_f32_e32 v82, 0x42700000, v82
	v_exp_f32_e32 v82, v82
	v_mul_f32_e32 v68, v61, v60
	v_add_f32_e32 v60, 1.0, v75
	v_rcp_f32_e32 v60, v60
	v_mov_b32_e32 v61, 0
	v_cvt_pk_fp8_f32 v61, v67, v68
	v_mul_f32_e32 v62, v62, v60
	v_add_f32_e32 v60, 1.0, v82
	v_rcp_f32_e32 v60, v60
	s_nop 0
	v_mul_f32_e32 v63, v63, v60
	v_mov_b32_e32 v60, 0
	v_cvt_pk_fp8_f32 v60, v11, v64
	v_cvt_pk_fp8_f32 v61, v62, v63 op_sel:[0,0,1]
	v_cvt_pk_f32_fp8_sdwa v[62:63], v80 src0_sel:WORD_1
	v_cvt_pk_fp8_f32 v60, v65, v66 op_sel:[0,0,1]
	v_cvt_pk_f32_fp8_e32 v[64:65], v81
	v_cvt_pk_f32_fp8_sdwa v[66:67], v81 src0_sel:WORD_1
	global_store_dwordx2 v[70:71], v[60:61], off offset:128
	v_cvt_pk_f32_fp8_e32 v[60:61], v80
	v_mul_f32_e32 v11, 0xbfb8aa3b, v60
	v_min_f32_e32 v11, 0x42700000, v11
	v_exp_f32_e32 v11, v11
	v_mul_f32_e32 v60, 0xbfb8aa3b, v61
	v_min_f32_e32 v60, 0x42700000, v60
	v_exp_f32_e32 v60, v60
	v_add_f32_e32 v11, 1.0, v11
	v_rcp_f32_e32 v11, v11
	v_mul_f32_e32 v61, 0xbfb8aa3b, v62
	v_min_f32_e32 v61, 0x42700000, v61
	v_exp_f32_e32 v61, v61
	v_mul_f32_e32 v11, v56, v11
	v_add_f32_e32 v56, 1.0, v60
	v_rcp_f32_e32 v56, v56
	v_mul_f32_e32 v62, 0xbfb8aa3b, v63
	v_min_f32_e32 v62, 0x42700000, v62
	v_exp_f32_e32 v62, v62
	v_mul_f32_e32 v56, v57, v56
	v_add_f32_e32 v57, 1.0, v61
	v_rcp_f32_e32 v57, v57
	v_mul_f32_e32 v63, 0xbfb8aa3b, v64
	v_min_f32_e32 v63, 0x42700000, v63
	v_exp_f32_e32 v63, v63
	v_mul_f32_e32 v57, v58, v57
	v_add_f32_e32 v58, 1.0, v62
	v_rcp_f32_e32 v58, v58
	v_mul_f32_e32 v64, 0xbfb8aa3b, v65
	v_min_f32_e32 v64, 0x42700000, v64
	v_exp_f32_e32 v64, v64
	v_mul_f32_e32 v58, v59, v58
	v_add_f32_e32 v59, 1.0, v63
	v_rcp_f32_e32 v59, v59
	v_mul_f32_e32 v65, 0xbfb8aa3b, v66
	v_min_f32_e32 v65, 0x42700000, v65
	v_exp_f32_e32 v65, v65
	v_mul_f32_e32 v59, v52, v59
	v_add_f32_e32 v52, 1.0, v64
	v_rcp_f32_e32 v52, v52
	v_mul_f32_e32 v66, 0xbfb8aa3b, v67
	v_min_f32_e32 v66, 0x42700000, v66
	v_exp_f32_e32 v66, v66
	v_mul_f32_e32 v60, v53, v52
	v_add_f32_e32 v52, 1.0, v65
	v_rcp_f32_e32 v52, v52
	v_mov_b32_e32 v53, 0
	v_cvt_pk_fp8_f32 v53, v59, v60
	v_cvt_pk_f32_fp8_sdwa v[60:61], v79 src0_sel:WORD_1
	v_mul_f32_e32 v54, v54, v52
	v_add_f32_e32 v52, 1.0, v66
	v_rcp_f32_e32 v52, v52
	s_nop 0
	v_mul_f32_e32 v55, v55, v52
	v_mov_b32_e32 v52, 0
	v_cvt_pk_fp8_f32 v52, v11, v56
	v_cvt_pk_fp8_f32 v53, v54, v55 op_sel:[0,0,1]
	v_lshl_add_u64 v[54:55], v[2:3], 0, s[0:1]
	s_mov_b32 s0, 0x24000
	v_cvt_pk_fp8_f32 v52, v57, v58 op_sel:[0,0,1]
	v_add_co_u32_e32 v56, vcc, s0, v2
	v_cvt_pk_f32_fp8_e32 v[58:59], v79
	s_nop 0
	v_addc_co_u32_e32 v57, vcc, 0, v3, vcc
	global_store_dwordx2 v[56:57], v[52:53], off
	v_cvt_pk_f32_fp8_e32 v[52:53], v78
	v_cvt_pk_f32_fp8_sdwa v[56:57], v78 src0_sel:WORD_1
	s_mov_b64 s[0:1], 0x28000
	v_mul_f32_e32 v11, 0xbfb8aa3b, v52
	v_min_f32_e32 v11, 0x42700000, v11
	v_exp_f32_e32 v11, v11
	v_mul_f32_e32 v52, 0xbfb8aa3b, v53
	v_min_f32_e32 v52, 0x42700000, v52
	v_exp_f32_e32 v52, v52
	v_add_f32_e32 v11, 1.0, v11
	v_rcp_f32_e32 v11, v11
	v_mul_f32_e32 v53, 0xbfb8aa3b, v56
	v_min_f32_e32 v53, 0x42700000, v53
	v_exp_f32_e32 v53, v53
	v_mul_f32_e32 v11, v48, v11
	v_add_f32_e32 v48, 1.0, v52
	v_rcp_f32_e32 v48, v48
	v_mul_f32_e32 v56, 0xbfb8aa3b, v57
	v_min_f32_e32 v56, 0x42700000, v56
	v_exp_f32_e32 v56, v56
	v_mul_f32_e32 v48, v49, v48
	v_add_f32_e32 v49, 1.0, v53
	v_rcp_f32_e32 v49, v49
	v_mul_f32_e32 v57, 0xbfb8aa3b, v58
	v_min_f32_e32 v57, 0x42700000, v57
	v_exp_f32_e32 v57, v57
	v_mul_f32_e32 v49, v50, v49
	v_add_f32_e32 v50, 1.0, v56
	v_rcp_f32_e32 v50, v50
	v_mul_f32_e32 v58, 0xbfb8aa3b, v59
	v_min_f32_e32 v58, 0x42700000, v58
	v_exp_f32_e32 v58, v58
	v_mul_f32_e32 v50, v51, v50
	v_add_f32_e32 v51, 1.0, v57
	v_rcp_f32_e32 v51, v51
	v_mul_f32_e32 v59, 0xbfb8aa3b, v60
	v_min_f32_e32 v59, 0x42700000, v59
	v_exp_f32_e32 v59, v59
	v_mul_f32_e32 v51, v44, v51
	v_add_f32_e32 v44, 1.0, v58
	v_rcp_f32_e32 v44, v44
	v_mul_f32_e32 v60, 0xbfb8aa3b, v61
	v_min_f32_e32 v60, 0x42700000, v60
	v_exp_f32_e32 v60, v60
	v_mul_f32_e32 v52, v45, v44
	v_add_f32_e32 v44, 1.0, v59
	v_rcp_f32_e32 v44, v44
	v_mov_b32_e32 v45, 0
	v_cvt_pk_fp8_f32 v45, v51, v52
	v_mul_f32_e32 v46, v46, v44
	v_add_f32_e32 v44, 1.0, v60
	v_rcp_f32_e32 v44, v44
	s_nop 0
	v_mul_f32_e32 v47, v47, v44
	v_mov_b32_e32 v44, 0
	v_cvt_pk_fp8_f32 v44, v11, v48
	v_cvt_pk_fp8_f32 v45, v46, v47 op_sel:[0,0,1]
	v_cvt_pk_f32_fp8_sdwa v[46:47], v76 src0_sel:WORD_1
	v_cvt_pk_fp8_f32 v44, v49, v50 op_sel:[0,0,1]
	v_cvt_pk_f32_fp8_e32 v[48:49], v77
	v_cvt_pk_f32_fp8_sdwa v[50:51], v77 src0_sel:WORD_1
	global_store_dwordx2 v[54:55], v[44:45], off offset:128
	v_cvt_pk_f32_fp8_e32 v[44:45], v76
	v_mul_f32_e32 v11, 0xbfb8aa3b, v44
	v_min_f32_e32 v11, 0x42700000, v11
	v_exp_f32_e32 v11, v11
	v_mul_f32_e32 v44, 0xbfb8aa3b, v45
	v_min_f32_e32 v44, 0x42700000, v44
	v_exp_f32_e32 v44, v44
	v_add_f32_e32 v11, 1.0, v11
	v_rcp_f32_e32 v11, v11
	v_mul_f32_e32 v45, 0xbfb8aa3b, v46
	v_min_f32_e32 v45, 0x42700000, v45
	v_exp_f32_e32 v45, v45
	v_mul_f32_e32 v11, v40, v11
	v_add_f32_e32 v40, 1.0, v44
	v_rcp_f32_e32 v40, v40
	v_mul_f32_e32 v46, 0xbfb8aa3b, v47
	v_min_f32_e32 v46, 0x42700000, v46
	v_exp_f32_e32 v46, v46
	v_mul_f32_e32 v40, v41, v40
	v_add_f32_e32 v41, 1.0, v45
	v_rcp_f32_e32 v41, v41
	v_mul_f32_e32 v47, 0xbfb8aa3b, v48
	v_min_f32_e32 v47, 0x42700000, v47
	v_exp_f32_e32 v47, v47
	v_mul_f32_e32 v41, v42, v41
	v_add_f32_e32 v42, 1.0, v46
	v_rcp_f32_e32 v42, v42
	v_mul_f32_e32 v48, 0xbfb8aa3b, v49
	v_min_f32_e32 v48, 0x42700000, v48
	v_exp_f32_e32 v48, v48
	v_mul_f32_e32 v42, v43, v42
	v_add_f32_e32 v43, 1.0, v47
	v_rcp_f32_e32 v43, v43
	v_mul_f32_e32 v49, 0xbfb8aa3b, v50
	v_min_f32_e32 v49, 0x42700000, v49
	v_exp_f32_e32 v49, v49
	v_mul_f32_e32 v43, v36, v43
	v_add_f32_e32 v36, 1.0, v48
	v_rcp_f32_e32 v36, v36
	v_mul_f32_e32 v50, 0xbfb8aa3b, v51
	v_min_f32_e32 v50, 0x42700000, v50
	v_exp_f32_e32 v50, v50
	v_mul_f32_e32 v44, v37, v36
	v_add_f32_e32 v36, 1.0, v49
	v_rcp_f32_e32 v36, v36
	v_mov_b32_e32 v37, 0
	v_cvt_pk_fp8_f32 v37, v43, v44
	v_mul_f32_e32 v38, v38, v36
	v_add_f32_e32 v36, 1.0, v50
	v_rcp_f32_e32 v36, v36
	s_nop 0
	v_mul_f32_e32 v39, v39, v36
	v_mov_b32_e32 v36, 0
	v_cvt_pk_fp8_f32 v36, v11, v40
	v_cvt_pk_fp8_f32 v37, v38, v39 op_sel:[0,0,1]
	v_lshl_add_u64 v[38:39], v[2:3], 0, s[0:1]
	s_mov_b32 s0, 0x28000
	v_cvt_pk_fp8_f32 v36, v41, v42 op_sel:[0,0,1]
	v_add_co_u32_e32 v40, vcc, s0, v2
	v_cvt_pk_f32_fp8_e32 v[42:43], v9
	s_nop 0
	v_addc_co_u32_e32 v41, vcc, 0, v3, vcc
	global_store_dwordx2 v[40:41], v[36:37], off
	v_cvt_pk_f32_fp8_e32 v[36:37], v8
	v_cvt_pk_f32_fp8_sdwa v[40:41], v8 src0_sel:WORD_1
	v_cvt_pk_f32_fp8_sdwa v[8:9], v9 src0_sel:WORD_1
	s_mov_b64 s[0:1], 0x2c000
	v_mul_f32_e32 v11, 0xbfb8aa3b, v36
	v_min_f32_e32 v11, 0x42700000, v11
	v_exp_f32_e32 v11, v11
	v_mul_f32_e32 v36, 0xbfb8aa3b, v37
	v_min_f32_e32 v36, 0x42700000, v36
	v_exp_f32_e32 v36, v36
	v_add_f32_e32 v11, 1.0, v11
	v_rcp_f32_e32 v11, v11
	v_mul_f32_e32 v37, 0xbfb8aa3b, v40
	v_min_f32_e32 v37, 0x42700000, v37
	v_exp_f32_e32 v37, v37
	v_mul_f32_e32 v11, v32, v11
	v_add_f32_e32 v32, 1.0, v36
	v_rcp_f32_e32 v32, v32
	v_mul_f32_e32 v40, 0xbfb8aa3b, v41
	v_min_f32_e32 v40, 0x42700000, v40
	v_exp_f32_e32 v40, v40
	v_mul_f32_e32 v32, v33, v32
	v_add_f32_e32 v33, 1.0, v37
	v_rcp_f32_e32 v33, v33
	v_mul_f32_e32 v41, 0xbfb8aa3b, v42
	v_mul_f32_e32 v8, 0xbfb8aa3b, v8
	v_min_f32_e32 v41, 0x42700000, v41
	v_min_f32_e32 v8, 0x42700000, v8
	v_mul_f32_e32 v33, v34, v33
	v_add_f32_e32 v34, 1.0, v40
	v_exp_f32_e32 v41, v41
	v_exp_f32_e32 v8, v8
	v_rcp_f32_e32 v34, v34
	v_mul_f32_e32 v42, 0xbfb8aa3b, v43
	v_mul_f32_e32 v9, 0xbfb8aa3b, v9
	v_min_f32_e32 v42, 0x42700000, v42
	v_min_f32_e32 v9, 0x42700000, v9
	v_mul_f32_e32 v34, v35, v34
	v_add_f32_e32 v35, 1.0, v41
	v_add_f32_e32 v8, 1.0, v8
	v_exp_f32_e32 v42, v42
	v_exp_f32_e32 v9, v9
	v_rcp_f32_e32 v35, v35
	v_rcp_f32_e32 v8, v8
	v_mul_f32_e32 v28, v28, v35
	v_add_f32_e32 v35, 1.0, v42
	v_mul_f32_e32 v30, v30, v8
	v_add_f32_e32 v8, 1.0, v9
	v_rcp_f32_e32 v35, v35
	v_rcp_f32_e32 v8, v8
	v_mov_b32_e32 v9, 0
	v_mul_f32_e32 v29, v29, v35
	v_mul_f32_e32 v31, v31, v8
	v_mov_b32_e32 v8, 0
	v_cvt_pk_fp8_f32 v8, v11, v32
	v_cvt_pk_fp8_f32 v9, v28, v29
	v_cvt_pk_f32_fp8_sdwa v[28:29], v6 src0_sel:WORD_1
	v_cvt_pk_fp8_f32 v8, v33, v34 op_sel:[0,0,1]
	v_cvt_pk_fp8_f32 v9, v30, v31 op_sel:[0,0,1]
	v_cvt_pk_f32_fp8_e32 v[30:31], v7
	v_mul_f32_e32 v11, 0xbfb8aa3b, v28
	v_mul_f32_e32 v28, 0xbfb8aa3b, v29
	global_store_dwordx2 v[38:39], v[8:9], off offset:128
	v_cvt_pk_f32_fp8_e32 v[8:9], v6
	v_cvt_pk_f32_fp8_sdwa v[6:7], v7 src0_sel:WORD_1
	v_mul_f32_e32 v29, 0xbfb8aa3b, v30
	v_min_f32_e32 v29, 0x42700000, v29
	v_mul_f32_e32 v9, 0xbfb8aa3b, v9
	v_min_f32_e32 v9, 0x42700000, v9
	v_exp_f32_e32 v9, v9
	v_mul_f32_e32 v6, 0xbfb8aa3b, v6
	v_min_f32_e32 v6, 0x42700000, v6
	v_exp_f32_e32 v29, v29
	v_add_f32_e32 v9, 1.0, v9
	v_exp_f32_e32 v6, v6
	v_rcp_f32_e32 v9, v9
	v_mul_f32_e32 v8, 0xbfb8aa3b, v8
	v_min_f32_e32 v8, 0x42700000, v8
	v_mul_f32_e32 v30, 0xbfb8aa3b, v31
	v_mul_f32_e32 v7, 0xbfb8aa3b, v7
	v_exp_f32_e32 v8, v8
	v_min_f32_e32 v30, 0x42700000, v30
	v_min_f32_e32 v7, 0x42700000, v7
	v_mul_f32_e32 v9, v25, v9
	v_add_f32_e32 v25, 1.0, v29
	v_add_f32_e32 v6, 1.0, v6
	v_exp_f32_e32 v30, v30
	v_exp_f32_e32 v7, v7
	v_rcp_f32_e32 v25, v25
	v_rcp_f32_e32 v6, v6
	v_min_f32_e32 v11, 0x42700000, v11
	v_min_f32_e32 v28, 0x42700000, v28
	v_add_f32_e32 v8, 1.0, v8
	v_exp_f32_e32 v11, v11
	v_exp_f32_e32 v28, v28
	v_rcp_f32_e32 v8, v8
	v_mul_f32_e32 v20, v20, v25
	v_add_f32_e32 v25, 1.0, v30
	v_mul_f32_e32 v22, v22, v6
	v_add_f32_e32 v6, 1.0, v7
	v_rcp_f32_e32 v25, v25
	v_rcp_f32_e32 v6, v6
	v_mul_f32_e32 v8, v24, v8
	v_add_f32_e32 v11, 1.0, v11
	v_add_f32_e32 v24, 1.0, v28
	v_rcp_f32_e32 v11, v11
	v_rcp_f32_e32 v24, v24
	v_mul_f32_e32 v21, v21, v25
	v_mul_f32_e32 v23, v23, v6
	v_mov_b32_e32 v6, 0
	v_mov_b32_e32 v7, 0
	v_cvt_pk_fp8_f32 v6, v8, v9
	v_cvt_pk_fp8_f32 v7, v20, v21
	v_mul_f32_e32 v11, v26, v11
	v_mul_f32_e32 v24, v27, v24
	v_cvt_pk_fp8_f32 v6, v11, v24 op_sel:[0,0,1]
	v_cvt_pk_fp8_f32 v7, v22, v23 op_sel:[0,0,1]
	v_lshl_add_u64 v[8:9], v[2:3], 0, s[0:1]
	s_mov_b32 s0, 0x2c000
	v_add_co_u32_e32 v2, vcc, s0, v2
	v_cvt_pk_f32_fp8_e32 v[20:21], v5
	s_nop 0
	v_addc_co_u32_e32 v3, vcc, 0, v3, vcc
	global_store_dwordx2 v[2:3], v[6:7], off
	v_cvt_pk_f32_fp8_e32 v[2:3], v4
	v_cvt_pk_f32_fp8_sdwa v[6:7], v4 src0_sel:WORD_1
	v_mul_f32_e32 v11, 0xbfb8aa3b, v20
	v_min_f32_e32 v11, 0x42700000, v11
	v_mul_f32_e32 v2, 0xbfb8aa3b, v2
	v_min_f32_e32 v2, 0x42700000, v2
	v_exp_f32_e32 v2, v2
	v_mul_f32_e32 v3, 0xbfb8aa3b, v3
	v_min_f32_e32 v3, 0x42700000, v3
	v_exp_f32_e32 v3, v3
	v_add_f32_e32 v2, 1.0, v2
	v_rcp_f32_e32 v2, v2
	v_mul_f32_e32 v6, 0xbfb8aa3b, v6
	v_min_f32_e32 v6, 0x42700000, v6
	v_exp_f32_e32 v6, v6
	v_mul_f32_e32 v16, v16, v2
	v_add_f32_e32 v2, 1.0, v3
	v_rcp_f32_e32 v2, v2
	v_mul_f32_e32 v7, 0xbfb8aa3b, v7
	v_min_f32_e32 v7, 0x42700000, v7
	v_exp_f32_e32 v7, v7
	v_mul_f32_e32 v3, v17, v2
	v_add_f32_e32 v2, 1.0, v6
	v_rcp_f32_e32 v2, v2
	v_exp_f32_e32 v11, v11
	v_mul_f32_e32 v20, 0xbfb8aa3b, v21
	v_cvt_pk_f32_fp8_sdwa v[4:5], v5 src0_sel:WORD_1
	v_mul_f32_e32 v6, v18, v2
	v_add_f32_e32 v2, 1.0, v7
	v_rcp_f32_e32 v2, v2
	v_min_f32_e32 v20, 0x42700000, v20
	v_exp_f32_e32 v20, v20
	v_mul_f32_e32 v4, 0xbfb8aa3b, v4
	v_mul_f32_e32 v7, v19, v2
	v_add_f32_e32 v2, 1.0, v11
	v_rcp_f32_e32 v2, v2
	v_min_f32_e32 v4, 0x42700000, v4
	v_exp_f32_e32 v4, v4
	v_mul_f32_e32 v5, 0xbfb8aa3b, v5
	v_mul_f32_e32 v11, v12, v2
	v_add_f32_e32 v2, 1.0, v20
	v_rcp_f32_e32 v2, v2
	v_min_f32_e32 v5, 0x42700000, v5
	v_exp_f32_e32 v5, v5
	s_mov_b64 s[0:1], -1
	v_mul_f32_e32 v12, v13, v2
	v_add_f32_e32 v2, 1.0, v4
	v_rcp_f32_e32 v2, v2
	s_and_b64 vcc, exec, s[6:7]
	v_mul_f32_e32 v4, v14, v2
	v_add_f32_e32 v2, 1.0, v5
	v_rcp_f32_e32 v2, v2
	s_nop 0
	v_mul_f32_e32 v5, v15, v2
	v_mov_b32_e32 v2, 0
	v_cvt_pk_fp8_f32 v2, v16, v3
	v_mov_b32_e32 v3, 0
	v_cvt_pk_fp8_f32 v3, v11, v12
	v_cvt_pk_fp8_f32 v2, v6, v7 op_sel:[0,0,1]
	v_cvt_pk_fp8_f32 v3, v4, v5 op_sel:[0,0,1]
	global_store_dwordx2 v[8:9], v[2:3], off offset:128
	s_cbranch_vccnz .LBB0_877
	s_andn2_b64 vcc, exec, s[22:23]
	s_cbranch_vccnz .LBB0_876
	s_barrier
	s_branch .LBB0_876
